# P5 epilogue: row loads software-pipelined one pass ahead (second register set, vmcnt(4)), 16-lane sums via DPP instead of ds_bpermute; on top of v74
# baseline (speedup 1.0000x reference)
; #define VM_WAIT() asm volatile("s_waitcnt vmcnt(0)" ::: "memory")
; __global__ void __launch_bounds__(NWAVES * 64, 2) fwd_kernel(Args a_unused) {
;     ...
;         for (int it = vcu; it < 8 * 32; it += G) { const int hh = it >> 5, segF = 1 + (it & 31);
;             scan_segment<true>(lds, PROJ, hh, segF, NSEG - segF, Lbuf, Dlog, OSCR);
;             VM_WAIT(); __syncthreads();
;             { const int l16 = lane & 15, tq = lane >> 4; const f32x4 hg0 = *(const f32x4*)(A->hgrn_g + hh * 128 + 8 * l16), hg1 = *(const f32x4*)(A->hgrn_g + hh * 128 + 8 * l16 + 4);
;               for (int i0 = wave * 64; i0 < wave * 64 + 64; i0 += 16) {
;                 u32x4 fw[4], bw[4], gq[4];
; #pragma unroll
;                 for (int b = 0; b < 4; ++b) { const int row = (segF - 1) * 512 + i0 + 4 * b + tq;
;                     fw[b] = *(const u32x4*)(OSCR + ((size_t)hh * NTOK + row) * 128 + 8 * l16); bw[b] = *(const u32x4*)(OSCR + ((size_t)(8 + hh) * NTOK + row) * 128 + 8 * l16);
;                     gq[b] = *(const u32x4*)(PROJ + PO_BG + ((size_t)hh * MROWS + row) * 128 + 8 * l16); }
.LBB0_1395:
	s_waitcnt vmcnt(0) lgkmcnt(0)
	s_barrier
	s_waitcnt vmcnt(0)
	s_barrier
	s_load_dwordx2 s[38:39], s[64:65], 0x60
	s_lshl_b32 s72, s42, 7
	s_ashr_i32 s73, s72, 31
	s_and_b32 s3, s92, 31
	s_lshl_b64 s[44:45], s[72:73], 2
	s_waitcnt lgkmcnt(0)
	s_add_u32 s38, s38, s44
	s_addc_u32 s39, s39, s45
	v_lshlrev_b32_e32 v6, 2, v150
	global_load_dwordx4 v[2:5], v6, s[38:39]
	s_nop 0
	global_load_dwordx4 v[6:9], v6, s[38:39] offset:16
	v_and_b32_e32 v15, 64, v174
	v_xor_b32_e32 v14, 1, v174
	v_add_u32_e32 v15, 64, v15
	v_cmp_lt_i32_e32 vcc, v14, v15
	s_lshl_b64 s[38:39], s[42:43], 22
	v_lshl_add_u64 v[10:11], v[154:155], 0, s[38:39]
	v_cndmask_b32_e32 v14, v174, v14, vcc
	v_lshlrev_b32_e32 v33, 2, v14
	v_xor_b32_e32 v14, 2, v174
	v_cmp_lt_i32_e32 vcc, v14, v15
	s_mov_b64 s[38:39], 0x2000000
	v_lshl_or_b32 v32, s3, 9, v163
	v_cndmask_b32_e32 v14, v174, v14, vcc
	v_lshlrev_b32_e32 v34, 2, v14
	v_xor_b32_e32 v14, 4, v174
	v_cmp_lt_i32_e32 vcc, v14, v15
	v_lshl_add_u64 v[12:13], v[10:11], 0, s[38:39]
	s_mul_hi_i32 s75, s42, 0x4100
	v_cndmask_b32_e32 v14, v174, v14, vcc
	v_lshlrev_b32_e32 v35, 2, v14
	v_xor_b32_e32 v14, 8, v174
	v_cmp_lt_i32_e32 vcc, v14, v15
	s_mul_i32 s74, s42, 0x4100
	s_mov_b32 s76, s88
	v_cndmask_b32_e32 v14, v174, v14, vcc
	v_lshlrev_b32_e32 v36, 2, v14
	v_add_u32_e32 v186, s76, v32
	v_add_u32_e32 v188, 16, v186
	v_add_u32_e32 v190, 20, v186
	v_add_u32_e32 v192, 24, v186
	v_add_u32_e32 v186, 28, v186
	v_ashrrev_i32_e32 v189, 31, v188
	v_ashrrev_i32_e32 v191, 31, v190
	v_ashrrev_i32_e32 v193, 31, v192
	v_ashrrev_i32_e32 v187, 31, v186
	v_lshlrev_b64 v[206:207], 8, v[188:189]
	v_lshl_add_u64 v[208:209], s[74:75], 0, v[188:189]
	v_lshlrev_b64 v[210:211], 8, v[190:191]
	v_lshl_add_u64 v[212:213], s[74:75], 0, v[190:191]
	v_lshlrev_b64 v[214:215], 8, v[192:193]
	v_lshl_add_u64 v[216:217], s[74:75], 0, v[192:193]
	v_lshlrev_b64 v[218:219], 8, v[186:187]
	v_lshl_add_u64 v[220:221], s[74:75], 0, v[186:187]
	v_lshl_add_u64 v[222:223], v[10:11], 0, v[206:207]
	v_lshl_add_u64 v[206:207], v[12:13], 0, v[206:207]
	v_lshlrev_b64 v[230:231], 8, v[208:209]
	v_lshl_add_u64 v[224:225], v[12:13], 0, v[210:211]
	v_lshlrev_b64 v[232:233], 8, v[212:213]
	v_lshl_add_u64 v[226:227], v[10:11], 0, v[214:215]
	v_lshl_add_u64 v[228:229], v[12:13], 0, v[214:215]
	v_lshlrev_b64 v[236:237], 8, v[216:217]
	v_lshl_add_u64 v[238:239], v[12:13], 0, v[218:219]
	v_lshlrev_b64 v[240:241], 8, v[220:221]
	v_lshl_add_u64 v[234:235], v[10:11], 0, v[210:211]
	v_lshl_add_u64 v[246:247], v[10:11], 0, v[218:219]
	global_load_dwordx4 v[206:209], v[206:207], off
	s_nop 0
	global_load_dwordx4 v[210:213], v[222:223], off
	global_load_dwordx4 v[214:217], v[224:225], off
	global_load_dwordx4 v[218:221], v[228:229], off
	s_nop 0
	global_load_dwordx4 v[222:225], v[226:227], off
	s_nop 0
	global_load_dwordx4 v[226:229], v[238:239], off
	v_lshl_add_u64 v[230:231], v[156:157], 0, v[230:231]
	v_lshl_add_u64 v[238:239], v[156:157], 0, v[232:233]
	v_lshl_add_u64 v[242:243], v[156:157], 0, v[236:237]
	v_lshl_add_u64 v[250:251], v[156:157], 0, v[240:241]
	global_load_dwordx4 v[230:233], v[230:231], off
	s_nop 0
	global_load_dwordx4 v[234:237], v[234:235], off
	s_nop 0
	global_load_dwordx4 v[238:241], v[238:239], off
	s_nop 0
	global_load_dwordx4 v[242:245], v[242:243], off
	s_nop 0
	global_load_dwordx4 v[246:249], v[246:247], off
	s_nop 0
	global_load_dwordx4 v[250:253], v[250:251], off
	s_waitcnt vmcnt(0)
.LBB0_1396:
	v_add_u32_e32 v22, s76, v32
	v_add_u32_e32 v24, 16, v22
	v_add_u32_e32 v26, 20, v22
	v_add_u32_e32 v28, 24, v22
	v_add_u32_e32 v22, 28, v22
	v_ashrrev_i32_e32 v25, 31, v24
	v_ashrrev_i32_e32 v27, 31, v26
	v_ashrrev_i32_e32 v29, 31, v28
	v_ashrrev_i32_e32 v23, 31, v22
	s_waitcnt vmcnt(4)
	v_mov_b64_e32 v[38:39], v[206:207]
	v_mov_b64_e32 v[40:41], v[208:209]
	v_mov_b64_e32 v[42:43], v[210:211]
	v_mov_b64_e32 v[44:45], v[212:213]
	v_mov_b64_e32 v[46:47], v[214:215]
	v_mov_b64_e32 v[48:49], v[216:217]
	v_mov_b64_e32 v[50:51], v[218:219]
	v_mov_b64_e32 v[52:53], v[220:221]
	v_mov_b64_e32 v[54:55], v[222:223]
	v_mov_b64_e32 v[56:57], v[224:225]
	v_mov_b64_e32 v[58:59], v[226:227]
	v_mov_b64_e32 v[60:61], v[228:229]
	v_mov_b64_e32 v[62:63], v[230:231]
	v_mov_b64_e32 v[64:65], v[232:233]
	v_mov_b64_e32 v[66:67], v[234:235]
	v_mov_b64_e32 v[68:69], v[236:237]
	v_mov_b64_e32 v[70:71], v[238:239]
	v_mov_b64_e32 v[72:73], v[240:241]
	v_mov_b64_e32 v[74:75], v[242:243]
	v_mov_b64_e32 v[76:77], v[244:245]
	v_mov_b64_e32 v[78:79], v[246:247]
	v_mov_b64_e32 v[80:81], v[248:249]
	v_mov_b64_e32 v[82:83], v[250:251]
	v_mov_b64_e32 v[84:85], v[252:253]
	s_add_i32 s38, s76, 16
	s_cmp_lt_i32 s38, s87
	s_cbranch_scc0 .Lp5e_last
	v_add_u32_e32 v186, s38, v32
	v_add_u32_e32 v188, 16, v186
	v_add_u32_e32 v190, 20, v186
	v_add_u32_e32 v192, 24, v186
	v_add_u32_e32 v186, 28, v186
	v_ashrrev_i32_e32 v189, 31, v188
	v_ashrrev_i32_e32 v191, 31, v190
	v_ashrrev_i32_e32 v193, 31, v192
	v_ashrrev_i32_e32 v187, 31, v186
	v_lshlrev_b64 v[206:207], 8, v[188:189]
	v_lshl_add_u64 v[208:209], s[74:75], 0, v[188:189]
	v_lshlrev_b64 v[210:211], 8, v[190:191]
	v_lshl_add_u64 v[212:213], s[74:75], 0, v[190:191]
	v_lshlrev_b64 v[214:215], 8, v[192:193]
	v_lshl_add_u64 v[216:217], s[74:75], 0, v[192:193]
	v_lshlrev_b64 v[218:219], 8, v[186:187]
	v_lshl_add_u64 v[220:221], s[74:75], 0, v[186:187]
	v_lshl_add_u64 v[222:223], v[10:11], 0, v[206:207]
	v_lshl_add_u64 v[206:207], v[12:13], 0, v[206:207]
	v_lshlrev_b64 v[230:231], 8, v[208:209]
	v_lshl_add_u64 v[224:225], v[12:13], 0, v[210:211]
	v_lshlrev_b64 v[232:233], 8, v[212:213]
	v_lshl_add_u64 v[226:227], v[10:11], 0, v[214:215]
	v_lshl_add_u64 v[228:229], v[12:13], 0, v[214:215]
	v_lshlrev_b64 v[236:237], 8, v[216:217]
	v_lshl_add_u64 v[238:239], v[12:13], 0, v[218:219]
	v_lshlrev_b64 v[240:241], 8, v[220:221]
	v_lshl_add_u64 v[234:235], v[10:11], 0, v[210:211]
	v_lshl_add_u64 v[246:247], v[10:11], 0, v[218:219]
	global_load_dwordx4 v[206:209], v[206:207], off
	s_nop 0
	global_load_dwordx4 v[210:213], v[222:223], off
	global_load_dwordx4 v[214:217], v[224:225], off
	global_load_dwordx4 v[218:221], v[228:229], off
	s_nop 0
	global_load_dwordx4 v[222:225], v[226:227], off
	s_nop 0
	global_load_dwordx4 v[226:229], v[238:239], off
	v_lshl_add_u64 v[230:231], v[156:157], 0, v[230:231]
	v_lshl_add_u64 v[238:239], v[156:157], 0, v[232:233]
	v_lshl_add_u64 v[242:243], v[156:157], 0, v[236:237]
	v_lshl_add_u64 v[250:251], v[156:157], 0, v[240:241]
	global_load_dwordx4 v[230:233], v[230:231], off
	s_nop 0
	global_load_dwordx4 v[234:237], v[234:235], off
	s_nop 0
	global_load_dwordx4 v[238:241], v[238:239], off
	s_nop 0
	global_load_dwordx4 v[242:245], v[242:243], off
	s_nop 0
	global_load_dwordx4 v[246:249], v[246:247], off
	s_nop 0
	global_load_dwordx4 v[250:253], v[250:251], off
; DI float bflo(unsigned w) { return __uint_as_float(w << 16); }
; DI float bfhi(unsigned w) { return __uint_as_float(w & 0xffff0000u); }
; __global__ void __launch_bounds__(NWAVES * 64, 2) fwd_kernel(Args a_unused) {
;     ...
;                 for (int b = 0; b < 4; ++b) { const int row = (segF - 1) * 512 + i0 + 4 * b + tq;
;                     fw[b] = *(const u32x4*)(OSCR + ((size_t)hh * NTOK + row) * 128 + 8 * l16); bw[b] = *(const u32x4*)(OSCR + ((size_t)(8 + hh) * NTOK + row) * 128 + 8 * l16);
;                     gq[b] = *(const u32x4*)(PROJ + PO_BG + ((size_t)hh * MROWS + row) * 128 + 8 * l16); }
; #pragma unroll
;                 for (int b = 0; b < 4; ++b) { const int row = (segF - 1) * 512 + i0 + 4 * b + tq;
;                     f32x4 o0, o1; o0[0] = bflo(fw[b].x) + bflo(bw[b].x); o0[1] = bfhi(fw[b].x) + bfhi(bw[b].x); o0[2] = bflo(fw[b].y) + bflo(bw[b].y); o0[3] = bfhi(fw[b].y) + bfhi(bw[b].y);
;                     o1[0] = bflo(fw[b].z) + bflo(bw[b].z); o1[1] = bfhi(fw[b].z) + bfhi(bw[b].z); o1[2] = bflo(fw[b].w) + bflo(bw[b].w); o1[3] = bfhi(fw[b].w) + bfhi(bw[b].w);
;                     float ss = o0[0] * o0[0] + o0[1] * o0[1] + o0[2] * o0[2] + o0[3] * o0[3] + o1[0] * o1[0] + o1[1] * o1[1] + o1[2] * o1[2] + o1[3] * o1[3];
.Lp5e_last:
	v_lshlrev_b64 v[24:25], 11, v[24:25]
	v_lshlrev_b64 v[22:23], 11, v[22:23]
	v_lshl_add_u64 v[24:25], s[66:67], 0, v[24:25]
	v_lshlrev_b64 v[26:27], 11, v[26:27]
	v_lshl_add_u64 v[22:23], s[66:67], 0, v[22:23]
	v_lshl_add_u64 v[24:25], v[24:25], 0, s[72:73]
	v_lshl_add_u64 v[26:27], s[66:67], 0, v[26:27]
	v_lshl_add_u64 v[22:23], v[22:23], 0, s[72:73]
	v_lshl_add_u64 v[24:25], v[24:25], 0, v[150:151]
	v_lshlrev_b64 v[28:29], 11, v[28:29]
	v_lshl_add_u64 v[26:27], v[26:27], 0, s[72:73]
	v_lshl_add_u64 v[86:87], v[22:23], 0, v[150:151]
	v_add_co_u32_e32 v22, vcc, s91, v24
	v_lshl_add_u64 v[28:29], s[66:67], 0, v[28:29]
	v_lshl_add_u64 v[26:27], v[26:27], 0, v[150:151]
	v_addc_co_u32_e32 v23, vcc, 0, v25, vcc
	v_lshl_add_u64 v[28:29], v[28:29], 0, s[72:73]
	v_add_co_u32_e32 v24, vcc, s91, v26
	v_lshl_add_u64 v[28:29], v[28:29], 0, v[150:151]
	s_nop 0
	v_addc_co_u32_e32 v25, vcc, 0, v27, vcc
	v_add_co_u32_e32 v26, vcc, s91, v28
	s_mov_b32 s38, 0x358637bd
	s_nop 0
	v_addc_co_u32_e32 v27, vcc, 0, v29, vcc
	v_add_co_u32_e32 v28, vcc, 0x4fc00000, v86
	v_mov_b64_e32 v[30:31], s[38:39]
	s_nop 0
	v_addc_co_u32_e32 v29, vcc, 0, v87, vcc
	v_mov_b32_e32 v14, 0
	v_mov_b32_e32 v15, 0
	v_mov_b32_e32 v16, 0
	v_mov_b32_e32 v17, 0
	v_mov_b32_e32 v18, 0
	v_mov_b32_e32 v19, 0
	v_mov_b32_e32 v20, 0
	v_mov_b32_e32 v21, 0
	s_add_i32 s76, s76, 16
	s_cmp_lt_i32 s76, s87
	v_lshlrev_b32_e32 v87, 16, v38
	v_lshlrev_b32_e32 v89, 16, v42
	v_and_b32_e32 v91, 0xffff0000, v38
	v_and_b32_e32 v93, 0xffff0000, v42
	v_lshlrev_b32_e32 v95, 16, v39
	v_lshlrev_b32_e32 v97, 16, v43
	v_and_b32_e32 v94, 0xffff0000, v39
	v_and_b32_e32 v96, 0xffff0000, v43
	v_lshlrev_b32_e32 v39, 16, v40
	v_lshlrev_b32_e32 v43, 16, v44
	v_and_b32_e32 v38, 0xffff0000, v40
	v_and_b32_e32 v42, 0xffff0000, v44
	v_lshlrev_b32_e32 v99, 16, v41
	v_lshlrev_b32_e32 v101, 16, v45
	v_and_b32_e32 v98, 0xffff0000, v41
	v_and_b32_e32 v100, 0xffff0000, v45
	v_and_b32_e32 v90, 0xffff0000, v46
	v_lshlrev_b32_e32 v41, 16, v47
	v_and_b32_e32 v40, 0xffff0000, v47
	v_lshlrev_b32_e32 v109, 16, v51
	v_lshlrev_b32_e32 v111, 16, v55
	v_and_b32_e32 v108, 0xffff0000, v51
	v_and_b32_e32 v110, 0xffff0000, v55
	v_pk_add_f32 v[38:39], v[42:43], v[38:39]
	v_pk_add_f32 v[42:43], v[100:101], v[98:99]
	v_lshlrev_b32_e32 v37, 16, v62
	v_and_b32_e32 v100, 0xffff0000, v62
	v_lshlrev_b32_e32 v101, 16, v63
	v_and_b32_e32 v116, 0xffff0000, v63
	v_and_b32_e32 v92, 0xffff0000, v66
	v_lshlrev_b32_e32 v63, 16, v67
	v_and_b32_e32 v62, 0xffff0000, v67
	v_lshlrev_b32_e32 v86, 16, v46
	v_lshlrev_b32_e32 v45, 16, v48
	v_and_b32_e32 v44, 0xffff0000, v48
	v_lshlrev_b32_e32 v47, 16, v49
	v_and_b32_e32 v46, 0xffff0000, v49
	v_lshlrev_b32_e32 v49, 16, v50
	v_lshlrev_b32_e32 v103, 16, v54
	v_and_b32_e32 v105, 0xffff0000, v50
	v_and_b32_e32 v107, 0xffff0000, v54
	v_lshlrev_b32_e32 v51, 16, v52
	v_lshlrev_b32_e32 v55, 16, v56
	v_and_b32_e32 v50, 0xffff0000, v52
	v_and_b32_e32 v54, 0xffff0000, v56
	v_lshlrev_b32_e32 v113, 16, v53
	v_lshlrev_b32_e32 v115, 16, v57
	v_and_b32_e32 v112, 0xffff0000, v53
	v_and_b32_e32 v114, 0xffff0000, v57
	v_lshlrev_b32_e32 v48, 16, v58
	v_and_b32_e32 v104, 0xffff0000, v58
	v_lshlrev_b32_e32 v53, 16, v59
	v_and_b32_e32 v52, 0xffff0000, v59
	v_lshlrev_b32_e32 v57, 16, v60
	v_and_b32_e32 v56, 0xffff0000, v60
	v_lshlrev_b32_e32 v59, 16, v61
	v_and_b32_e32 v58, 0xffff0000, v61
	v_pk_add_f32 v[60:61], v[96:97], v[94:95]
	v_lshlrev_b32_e32 v117, 16, v64
	v_and_b32_e32 v118, 0xffff0000, v64
	v_lshlrev_b32_e32 v119, 16, v65
	v_and_b32_e32 v120, 0xffff0000, v65
	v_lshlrev_b32_e32 v88, 16, v66
	v_lshlrev_b32_e32 v65, 16, v68
	v_and_b32_e32 v64, 0xffff0000, v68
	v_lshlrev_b32_e32 v67, 16, v69
	v_and_b32_e32 v66, 0xffff0000, v69
	v_lshlrev_b32_e32 v121, 16, v70
	v_and_b32_e32 v122, 0xffff0000, v70
	v_lshlrev_b32_e32 v123, 16, v71
	v_and_b32_e32 v124, 0xffff0000, v71
	v_lshlrev_b32_e32 v125, 16, v72
	v_and_b32_e32 v126, 0xffff0000, v72
	v_lshlrev_b32_e32 v127, 16, v73
	v_and_b32_e32 v128, 0xffff0000, v73
	v_pk_add_f32 v[68:69], v[110:111], v[108:109]
	v_lshlrev_b32_e32 v108, 16, v74
	v_and_b32_e32 v109, 0xffff0000, v74
	v_lshlrev_b32_e32 v110, 16, v75
	v_and_b32_e32 v111, 0xffff0000, v75
	v_and_b32_e32 v106, 0xffff0000, v78
	v_lshlrev_b32_e32 v71, 16, v79
	v_and_b32_e32 v70, 0xffff0000, v79
	v_lshlrev_b32_e32 v73, 16, v80
	v_and_b32_e32 v72, 0xffff0000, v80
	v_lshlrev_b32_e32 v75, 16, v81
	v_and_b32_e32 v74, 0xffff0000, v81
	v_lshlrev_b32_e32 v129, 16, v82
	v_and_b32_e32 v130, 0xffff0000, v82
	v_lshlrev_b32_e32 v131, 16, v83
	v_and_b32_e32 v132, 0xffff0000, v83
	v_pk_add_f32 v[40:41], v[62:63], v[40:41]
	v_pk_add_f32 v[82:83], v[92:93], v[90:91]
	v_pk_add_f32 v[50:51], v[54:55], v[50:51]
	v_pk_add_f32 v[54:55], v[114:115], v[112:113]
	v_lshlrev_b32_e32 v112, 16, v76
	v_and_b32_e32 v113, 0xffff0000, v76
	v_lshlrev_b32_e32 v114, 16, v77
	v_and_b32_e32 v115, 0xffff0000, v77
	v_lshlrev_b32_e32 v102, 16, v78
	v_pk_mul_f32 v[76:77], v[60:61], v[60:61]
	v_pk_add_f32 v[62:63], v[88:89], v[86:87]
	v_pk_add_f32 v[44:45], v[64:65], v[44:45]
	v_pk_add_f32 v[46:47], v[66:67], v[46:47]
	v_pk_add_f32 v[52:53], v[70:71], v[52:53]
	v_pk_add_f32 v[70:71], v[106:107], v[104:105]
	v_pk_add_f32 v[56:57], v[72:73], v[56:57]
	v_pk_add_f32 v[58:59], v[74:75], v[58:59]
	v_pk_mul_f32 v[72:73], v[40:41], v[40:41]
	v_pk_mul_f32 v[74:75], v[82:83], v[82:83]
	v_pk_mul_f32 v[78:79], v[38:39], v[38:39]
	v_pk_mul_f32 v[80:81], v[42:43], v[42:43]
	v_pk_mul_f32 v[64:65], v[68:69], v[68:69]
	v_pk_add_f32 v[48:49], v[102:103], v[48:49]
	v_mov_b32_e32 v87, v77
	v_pk_mul_f32 v[88:89], v[44:45], v[44:45]
	v_pk_mul_f32 v[90:91], v[46:47], v[46:47]
; DI float bflo(unsigned w) { return __uint_as_float(w << 16); }
; DI float bfhi(unsigned w) { return __uint_as_float(w & 0xffff0000u); }
; __global__ void __launch_bounds__(NWAVES * 64, 2) fwd_kernel(Args a_unused) {
;     ...
;                     float ss = o0[0] * o0[0] + o0[1] * o0[1] + o0[2] * o0[2] + o0[3] * o0[3] + o1[0] * o1[0] + o1[1] * o1[1] + o1[2] * o1[2] + o1[3] * o1[3];
;                     ss += __shfl_xor(ss, 1); ss += __shfl_xor(ss, 2); ss += __shfl_xor(ss, 4); ss += __shfl_xor(ss, 8);
;                     const float rstd = rsqrtf(ss * (1.0f / 128.0f) + EPS);
;                     int w0 = __builtin_amdgcn_cvt_pk_fp8_f32(o0[0] * rstd * hg0[0] * bflo(gq[b].x), o0[1] * rstd * hg0[1] * bfhi(gq[b].x), 0, false); w0 = __builtin_amdgcn_cvt_pk_fp8_f32(o0[2] * rstd * hg0[2] * bflo(gq[b].y), o0[3] * rstd * hg0[3] * bfhi(gq[b].y), w0, true);
;                     int w1 = __builtin_amdgcn_cvt_pk_fp8_f32(o1[0] * rstd * hg1[0] * bflo(gq[b].z), o1[1] * rstd * hg1[1] * bfhi(gq[b].z), 0, false); w1 = __builtin_amdgcn_cvt_pk_fp8_f32(o1[2] * rstd * hg1[2] * bflo(gq[b].w), o1[3] * rstd * hg1[3] * bfhi(gq[b].w), w1, true);
	v_pk_mul_f32 v[92:93], v[52:53], v[52:53]
	v_pk_mul_f32 v[94:95], v[70:71], v[70:71]
	v_pk_fma_f32 v[74:75], v[62:63], v[62:63], v[74:75]
	v_mov_b32_e32 v86, v73
	v_mov_b32_e32 v77, v79
	v_mov_b32_e32 v79, v81
	v_mov_b32_e32 v81, v65
	v_mov_b32_e32 v73, v76
	v_mov_b32_e32 v76, v89
	v_mov_b32_e32 v89, v78
	v_mov_b32_e32 v78, v91
	v_mov_b32_e32 v91, v80
	v_pk_fma_f32 v[94:95], v[48:49], v[48:49], v[94:95]
	v_mov_b32_e32 v80, v93
	v_pk_add_f32 v[74:75], v[74:75], v[86:87]
	v_pk_mul_f32 v[66:67], v[50:51], v[50:51]
	v_pk_mul_f32 v[96:97], v[56:57], v[56:57]
	v_mov_b32_e32 v93, v64
	v_pk_add_f32 v[80:81], v[94:95], v[80:81]
	v_pk_add_f32 v[72:73], v[72:73], v[74:75]
	v_mov_b32_e32 v65, v67
	v_mov_b32_e32 v64, v97
	v_pk_add_f32 v[74:75], v[92:93], v[80:81]
	v_pk_add_f32 v[72:73], v[76:77], v[72:73]
	v_lshlrev_b32_e32 v133, 16, v84
	v_and_b32_e32 v134, 0xffff0000, v84
	v_lshlrev_b32_e32 v135, 16, v85
	v_and_b32_e32 v136, 0xffff0000, v85
	v_pk_mul_f32 v[84:85], v[54:55], v[54:55]
	v_pk_mul_f32 v[98:99], v[58:59], v[58:59]
	v_mov_b32_e32 v97, v66
	v_pk_add_f32 v[64:65], v[64:65], v[74:75]
	v_pk_add_f32 v[72:73], v[88:89], v[72:73]
	v_mov_b32_e32 v67, v85
	v_mov_b32_e32 v66, v99
	v_pk_add_f32 v[64:65], v[96:97], v[64:65]
	v_pk_add_f32 v[72:73], v[78:79], v[72:73]
	v_mov_b32_e32 v99, v84
	v_pk_add_f32 v[64:65], v[66:67], v[64:65]
	v_pk_add_f32 v[66:67], v[90:91], v[72:73]
	v_pk_add_f32 v[64:65], v[98:99], v[64:65]
	s_nop 1
	v_add_f32_dpp v64, v64, v64 quad_perm:[1,0,3,2] row_mask:0xf bank_mask:0xf
	v_add_f32_dpp v65, v65, v65 quad_perm:[1,0,3,2] row_mask:0xf bank_mask:0xf
	v_add_f32_dpp v66, v66, v66 quad_perm:[1,0,3,2] row_mask:0xf bank_mask:0xf
	v_add_f32_dpp v67, v67, v67 quad_perm:[1,0,3,2] row_mask:0xf bank_mask:0xf
	s_nop 1
	v_add_f32_dpp v64, v64, v64 quad_perm:[2,3,0,1] row_mask:0xf bank_mask:0xf
	v_add_f32_dpp v65, v65, v65 quad_perm:[2,3,0,1] row_mask:0xf bank_mask:0xf
	v_add_f32_dpp v66, v66, v66 quad_perm:[2,3,0,1] row_mask:0xf bank_mask:0xf
	v_add_f32_dpp v67, v67, v67 quad_perm:[2,3,0,1] row_mask:0xf bank_mask:0xf
	s_nop 1
	v_add_f32_dpp v64, v64, v64 row_half_mirror row_mask:0xf bank_mask:0xf
	v_add_f32_dpp v65, v65, v65 row_half_mirror row_mask:0xf bank_mask:0xf
	v_add_f32_dpp v66, v66, v66 row_half_mirror row_mask:0xf bank_mask:0xf
	v_add_f32_dpp v67, v67, v67 row_half_mirror row_mask:0xf bank_mask:0xf
	s_nop 1
	v_add_f32_dpp v64, v64, v64 row_mirror row_mask:0xf bank_mask:0xf
	v_add_f32_dpp v65, v65, v65 row_mirror row_mask:0xf bank_mask:0xf
	v_add_f32_dpp v66, v66, v66 row_mirror row_mask:0xf bank_mask:0xf
	v_add_f32_dpp v67, v67, v67 row_mirror row_mask:0xf bank_mask:0xf
	s_nop 0
	v_pk_fma_f32 v[66:67], v[66:67], s[70:71], v[30:31] op_sel_hi:[1,0,0]
	v_cmp_gt_f32_e64 s[44:45], s90, v67
	v_pk_fma_f32 v[30:31], v[64:65], s[70:71], v[30:31] op_sel_hi:[1,0,0]
	v_mul_f32_e32 v64, 0x4b800000, v67
	v_mul_f32_e32 v65, 0x4b800000, v66
	v_cmp_gt_f32_e32 vcc, s90, v66
	v_mul_f32_e32 v72, 0x4b800000, v31
	v_mul_f32_e32 v73, 0x4b800000, v30
	v_cmp_gt_f32_e64 s[38:39], s90, v30
	v_cmp_gt_f32_e64 s[42:43], s90, v31
	v_cndmask_b32_e64 v64, v67, v64, s[44:45]
	v_cndmask_b32_e32 v65, v66, v65, vcc
	v_cndmask_b32_e64 v31, v31, v72, s[42:43]
	v_cndmask_b32_e64 v30, v30, v73, s[38:39]
	v_rsq_f32_e32 v64, v64
	v_rsq_f32_e32 v65, v65
	v_rsq_f32_e32 v31, v31
	v_rsq_f32_e32 v30, v30
	v_mul_f32_e32 v66, 0x45800000, v64
	v_mul_f32_e32 v67, 0x45800000, v65
	v_mul_f32_e32 v72, 0x45800000, v31
	v_mul_f32_e32 v73, 0x45800000, v30
	v_cndmask_b32_e64 v64, v64, v66, s[44:45]
	v_cndmask_b32_e32 v65, v65, v67, vcc
	v_cndmask_b32_e64 v31, v31, v72, s[42:43]
	v_cndmask_b32_e64 v30, v30, v73, s[38:39]
	v_mul_f32_e32 v63, v63, v64
	v_mul_f32_e32 v66, v83, v64
	v_mul_f32_e32 v39, v39, v64
	v_mul_f32_e32 v38, v38, v64
	v_mul_f32_e32 v61, v61, v64
; DI float bflo(unsigned w) { return __uint_as_float(w << 16); }
; DI float bfhi(unsigned w) { return __uint_as_float(w & 0xffff0000u); }
; __global__ void __launch_bounds__(NWAVES * 64, 2) fwd_kernel(Args a_unused) {
;     ...
;                     int w0 = __builtin_amdgcn_cvt_pk_fp8_f32(o0[0] * rstd * hg0[0] * bflo(gq[b].x), o0[1] * rstd * hg0[1] * bfhi(gq[b].x), 0, false); w0 = __builtin_amdgcn_cvt_pk_fp8_f32(o0[2] * rstd * hg0[2] * bflo(gq[b].y), o0[3] * rstd * hg0[3] * bfhi(gq[b].y), w0, true);
;                     int w1 = __builtin_amdgcn_cvt_pk_fp8_f32(o1[0] * rstd * hg1[0] * bflo(gq[b].z), o1[1] * rstd * hg1[1] * bfhi(gq[b].z), 0, false); w1 = __builtin_amdgcn_cvt_pk_fp8_f32(o1[2] * rstd * hg1[2] * bflo(gq[b].w), o1[3] * rstd * hg1[3] * bfhi(gq[b].w), w1, true);
;                     *(u32x2*)(YAB + (size_t)row * D + 1024 + hh * 128 + 8 * l16) = (u32x2){(unsigned)w0, (unsigned)w1}; } } }
;             __syncthreads();
;         }
	v_mul_f32_e32 v60, v60, v64
	v_mul_f32_e32 v43, v43, v64
	v_mul_f32_e32 v42, v42, v64
	v_mul_f32_e32 v62, v62, v65
	v_mul_f32_e32 v64, v82, v65
	v_mul_f32_e32 v41, v41, v65
	v_mul_f32_e32 v40, v40, v65
	v_mul_f32_e32 v45, v45, v65
	v_mul_f32_e32 v44, v44, v65
	v_mul_f32_e32 v47, v47, v65
	v_mul_f32_e32 v46, v46, v65
	v_mul_f32_e32 v49, v49, v31
	v_mul_f32_e32 v65, v71, v31
	v_mul_f32_e32 v67, v69, v31
	v_mul_f32_e32 v68, v68, v31
	v_mul_f32_e32 v51, v51, v31
	v_mul_f32_e32 v50, v50, v31
	v_mul_f32_e32 v55, v55, v31
	v_mul_f32_e32 v31, v54, v31
	v_mul_f32_e32 v48, v48, v30
	v_mul_f32_e32 v54, v70, v30
	v_mul_f32_e32 v53, v53, v30
	v_mul_f32_e32 v52, v52, v30
	v_mul_f32_e32 v57, v57, v30
	v_mul_f32_e32 v56, v56, v30
	v_mul_f32_e32 v59, v59, v30
	v_mul_f32_e32 v30, v58, v30
	v_mul_f32_e32 v58, v2, v63
	v_mul_f32_e32 v63, v3, v66
	v_mul_f32_e32 v39, v6, v39
	v_mul_f32_e32 v38, v7, v38
	v_mul_f32_e32 v62, v2, v62
	v_mul_f32_e32 v64, v3, v64
	v_mul_f32_e32 v45, v6, v45
	v_mul_f32_e32 v44, v7, v44
	v_mul_f32_e32 v37, v58, v37
	v_mul_f32_e32 v58, v63, v100
	v_mul_f32_e32 v39, v39, v117
	v_mul_f32_e32 v38, v38, v118
	v_mul_f32_e32 v49, v2, v49
	v_mul_f32_e32 v65, v3, v65
	v_mul_f32_e32 v51, v6, v51
	v_mul_f32_e32 v50, v7, v50
	v_mul_f32_e32 v62, v62, v121
	v_mul_f32_e32 v63, v64, v122
	v_mul_f32_e32 v45, v45, v125
	v_mul_f32_e32 v44, v44, v126
	v_cvt_pk_fp8_f32 v14, v37, v58
	v_cvt_pk_fp8_f32 v15, v39, v38
	v_mul_f32_e32 v48, v2, v48
	v_mul_f32_e32 v54, v3, v54
	v_mul_f32_e32 v57, v6, v57
	v_mul_f32_e32 v56, v7, v56
	v_mul_f32_e32 v49, v49, v108
	v_mul_f32_e32 v64, v65, v109
	v_mul_f32_e32 v51, v51, v112
	v_mul_f32_e32 v50, v50, v113
	v_cvt_pk_fp8_f32 v16, v62, v63
	v_cvt_pk_fp8_f32 v17, v45, v44
	v_mul_f32_e32 v61, v4, v61
	v_mul_f32_e32 v60, v5, v60
	v_mul_f32_e32 v43, v8, v43
	v_mul_f32_e32 v42, v9, v42
	v_mul_f32_e32 v48, v48, v129
	v_mul_f32_e32 v54, v54, v130
	v_mul_f32_e32 v57, v57, v133
	v_mul_f32_e32 v56, v56, v134
	v_cvt_pk_fp8_f32 v18, v49, v64
	v_cvt_pk_fp8_f32 v19, v51, v50
	v_mul_f32_e32 v41, v4, v41
	v_mul_f32_e32 v40, v5, v40
	v_mul_f32_e32 v47, v8, v47
	v_mul_f32_e32 v46, v9, v46
	v_mul_f32_e32 v61, v61, v101
	v_mul_f32_e32 v60, v60, v116
	v_mul_f32_e32 v43, v43, v119
	v_mul_f32_e32 v42, v42, v120
	v_cvt_pk_fp8_f32 v20, v48, v54
	v_cvt_pk_fp8_f32 v21, v57, v56
	v_mul_f32_e32 v66, v4, v67
	v_mul_f32_e32 v67, v5, v68
	v_mul_f32_e32 v55, v8, v55
	v_mul_f32_e32 v31, v9, v31
	v_mul_f32_e32 v41, v41, v123
	v_mul_f32_e32 v40, v40, v124
	v_mul_f32_e32 v47, v47, v127
	v_mul_f32_e32 v46, v46, v128
	v_cvt_pk_fp8_f32 v14, v61, v60 op_sel:[0,0,1]
	v_cvt_pk_fp8_f32 v15, v43, v42 op_sel:[0,0,1]
	v_mul_f32_e32 v53, v4, v53
	v_mul_f32_e32 v52, v5, v52
	v_mul_f32_e32 v59, v8, v59
	v_mul_f32_e32 v30, v9, v30
	v_mul_f32_e32 v65, v66, v110
	v_mul_f32_e32 v66, v67, v111
	v_mul_f32_e32 v55, v55, v114
	v_mul_f32_e32 v31, v31, v115
	v_cvt_pk_fp8_f32 v16, v41, v40 op_sel:[0,0,1]
	v_cvt_pk_fp8_f32 v17, v47, v46 op_sel:[0,0,1]
	v_mul_f32_e32 v53, v53, v131
	v_mul_f32_e32 v52, v52, v132
	v_mul_f32_e32 v59, v59, v135
	v_mul_f32_e32 v30, v30, v136
	v_cvt_pk_fp8_f32 v18, v65, v66 op_sel:[0,0,1]
	v_cvt_pk_fp8_f32 v19, v55, v31 op_sel:[0,0,1]
	v_cvt_pk_fp8_f32 v20, v53, v52 op_sel:[0,0,1]
	v_cvt_pk_fp8_f32 v21, v59, v30 op_sel:[0,0,1]
	global_store_dwordx2 v[22:23], v[14:15], off offset:1024
	global_store_dwordx2 v[24:25], v[16:17], off offset:1024
	global_store_dwordx2 v[26:27], v[18:19], off offset:1024
	global_store_dwordx2 v[28:29], v[20:21], off offset:1024
	s_cbranch_scc1 .LBB0_1396
	s_add_i32 s93, s93, s33
	s_add_i32 s92, s92, s33
	s_cmpk_lt_i32 s93, 0x100
	s_barrier
	s_cbranch_scc1 .LBB0_1377
	v_readlane_b32 s0, v254, 6
	v_readlane_b32 s96, v254, 9
	v_readlane_b32 s1, v254, 7
	v_readlane_b32 s97, v254, 10
	v_readlane_b32 s95, v254, 8
